# speedup vs baseline: 1.0251x; 1.0101x over previous
.LBB0_48:
	v_add_f32_e32 v2, v243, v2
	v_mov_b32_e32 v4, v2
	s_nop 1
	v_permlane32_swap_b32_e32 v2, v4
	v_add_f32_e32 v2, v2, v4
	v_div_scale_f32 v4, s[4:5], v2, v2, 1.0
	v_rcp_f32_e32 v5, v4
	v_mov_b32_e32 v6, v229
	v_fma_f32 v8, -v4, v5, 1.0
	v_fmac_f32_e32 v5, v8, v5
	v_div_scale_f32 v8, vcc, 1.0, v2, 1.0
	v_mul_f32_e32 v9, v8, v5
	v_fma_f32 v10, -v4, v9, v8
	v_fmac_f32_e32 v9, v10, v5
	v_fma_f32 v4, -v4, v9, v8
	v_div_fmas_f32 v4, v4, v5, v9
	v_lshlrev_b32_e32 v5, 8, v6
	v_ashrrev_i32_e32 v7, 5, v6
	v_and_b32_e32 v5, 0x1f00, v5
	v_div_fixup_f32 v2, v4, v2, 1.0
	v_add_u32_e32 v4, 8, v7
	v_add_u32_e32 v5, s84, v5
	v_bitop3_b32 v12, v7, v6, 15 bitop3:0x78
	v_pk_mul_f32 v[8:9], v[2:3], v[130:131] op_sel_hi:[0,1]
	v_pk_mul_f32 v[10:11], v[2:3], v[132:133] op_sel_hi:[0,1]
	v_lshl_add_u32 v12, v12, 4, v5
	v_bitop3_b32 v4, v4, v6, 15 bitop3:0x78
	ds_write_b128 v12, v[8:11]
	v_pk_mul_f32 v[8:9], v[2:3], v[114:115] op_sel_hi:[0,1]
	v_pk_mul_f32 v[10:11], v[2:3], v[116:117] op_sel_hi:[0,1]
	v_lshl_add_u32 v4, v4, 4, v5
	ds_write_b128 v4, v[8:11]
	v_add_u32_e32 v4, 2, v7
	v_bitop3_b32 v4, v4, v6, 15 bitop3:0x78
	v_add_u32_e32 v12, 10, v7
	v_pk_mul_f32 v[8:9], v[2:3], v[134:135] op_sel_hi:[0,1]
	v_pk_mul_f32 v[10:11], v[2:3], v[136:137] op_sel_hi:[0,1]
	v_lshl_add_u32 v4, v4, 4, v5
	ds_write_b128 v4, v[8:11]
	v_bitop3_b32 v4, v12, v6, 15 bitop3:0x78
	v_pk_mul_f32 v[8:9], v[2:3], v[118:119] op_sel_hi:[0,1]
	v_pk_mul_f32 v[10:11], v[2:3], v[120:121] op_sel_hi:[0,1]
	v_lshl_add_u32 v4, v4, 4, v5
	ds_write_b128 v4, v[8:11]
	v_add_u32_e32 v4, 4, v7
	v_bitop3_b32 v4, v4, v6, 15 bitop3:0x78
	v_add_u32_e32 v12, 12, v7
	v_pk_mul_f32 v[8:9], v[2:3], v[138:139] op_sel_hi:[0,1]
	v_pk_mul_f32 v[10:11], v[2:3], v[140:141] op_sel_hi:[0,1]
	v_lshl_add_u32 v4, v4, 4, v5
	ds_write_b128 v4, v[8:11]
	v_bitop3_b32 v4, v12, v6, 15 bitop3:0x78
	v_pk_mul_f32 v[8:9], v[2:3], v[122:123] op_sel_hi:[0,1]
	v_pk_mul_f32 v[10:11], v[2:3], v[124:125] op_sel_hi:[0,1]
	v_lshl_add_u32 v4, v4, 4, v5
	ds_write_b128 v4, v[8:11]
	v_add_u32_e32 v4, 6, v7
	v_bitop3_b32 v4, v4, v6, 15 bitop3:0x78
	v_add_u32_e32 v7, 14, v7
	v_pk_mul_f32 v[8:9], v[2:3], v[142:143] op_sel_hi:[0,1]
	v_pk_mul_f32 v[10:11], v[2:3], v[144:145] op_sel_hi:[0,1]
	v_lshl_add_u32 v4, v4, 4, v5
	ds_write_b128 v4, v[8:11]
	v_pk_mul_f32 v[8:9], v[2:3], v[126:127] op_sel_hi:[0,1]
	v_pk_mul_f32 v[10:11], v[2:3], v[128:129] op_sel_hi:[0,1]
	v_bitop3_b32 v2, v7, v6, 15 bitop3:0x78
	v_lshl_add_u32 v2, v2, 4, v5
	ds_write_b128 v2, v[8:11]
	v_lshlrev_b32_e32 v2, 2, v6
	v_ashrrev_i32_e32 v7, 4, v6
	v_and_or_b32 v2, v2, 60, s90
	v_lshl_add_u64 v[4:5], v[2:3], 2, s[72:73]
	v_add_u32_e32 v2, s88, v7
	v_xor_b32_e32 v8, v7, v6
	v_cmp_gt_i32_e32 vcc, s3, v2
	v_lshlrev_b32_e32 v8, 4, v8
	s_and_saveexec_b64 s[4:5], vcc
	s_cbranch_execz .LBB0_50
	v_lshlrev_b32_e32 v9, 8, v7
	v_and_b32_e32 v10, 0xf0, v8
	v_add3_u32 v9, s84, v9, v10
	ds_read_b128 v[10:13], v9
	v_add_lshl_u32 v2, v2, s76, 10
	v_lshl_add_u64 v[14:15], v[2:3], 2, v[4:5]
	s_waitcnt lgkmcnt(0)
	global_store_dwordx4 v[14:15], v[10:13], off sc0 sc1
.LBB0_50:
	s_or_b64 exec, exec, s[4:5]
	v_add_u32_e32 v9, 4, v7
	v_add_u32_e32 v2, s88, v9
	v_cmp_gt_i32_e32 vcc, s3, v2
	s_and_saveexec_b64 s[4:5], vcc
	s_cbranch_execz .LBB0_52
	v_lshlrev_b32_e32 v10, 8, v9
	v_xor_b32_e32 v9, v9, v6
	v_lshlrev_b32_e32 v9, 4, v9
	v_and_b32_e32 v9, 0xf0, v9
	v_add3_u32 v9, s84, v10, v9
	ds_read_b128 v[10:13], v9
	v_add_lshl_u32 v2, v2, s76, 10
	v_lshl_add_u64 v[14:15], v[2:3], 2, v[4:5]
	s_waitcnt lgkmcnt(0)
	global_store_dwordx4 v[14:15], v[10:13], off sc0 sc1
.LBB0_52:
	s_or_b64 exec, exec, s[4:5]
	v_add_u32_e32 v9, 8, v7
	v_add_u32_e32 v2, s88, v9
	v_cmp_gt_i32_e32 vcc, s3, v2
	s_and_saveexec_b64 s[4:5], vcc
	s_cbranch_execz .LBB0_54
	v_lshlrev_b32_e32 v10, 8, v9
	v_xor_b32_e32 v9, v9, v6
	v_lshlrev_b32_e32 v9, 4, v9
	v_and_b32_e32 v9, 0xf0, v9
	v_add3_u32 v9, s84, v10, v9
	ds_read_b128 v[10:13], v9
	v_add_lshl_u32 v2, v2, s76, 10
	v_lshl_add_u64 v[14:15], v[2:3], 2, v[4:5]
	s_waitcnt lgkmcnt(0)
	global_store_dwordx4 v[14:15], v[10:13], off sc0 sc1
.LBB0_54:
	s_or_b64 exec, exec, s[4:5]
	v_add_u32_e32 v9, 12, v7
	v_add_u32_e32 v2, s88, v9
	v_cmp_gt_i32_e32 vcc, s3, v2
	s_and_saveexec_b64 s[4:5], vcc
	s_cbranch_execz .LBB0_56
	v_lshlrev_b32_e32 v10, 8, v9
	v_xor_b32_e32 v9, v9, v6
	v_lshlrev_b32_e32 v9, 4, v9
	v_and_b32_e32 v9, 0xf0, v9
	v_add3_u32 v9, s84, v10, v9
	ds_read_b128 v[10:13], v9
	v_add_lshl_u32 v2, v2, s76, 10
	v_lshl_add_u64 v[14:15], v[2:3], 2, v[4:5]
	s_waitcnt lgkmcnt(0)
	global_store_dwordx4 v[14:15], v[10:13], off sc0 sc1
.LBB0_56:
	s_or_b64 exec, exec, s[4:5]
	v_add_u32_e32 v9, 16, v7
	v_add_u32_e32 v2, s88, v9
	v_cmp_gt_i32_e32 vcc, s3, v2
	s_and_saveexec_b64 s[4:5], vcc
	s_cbranch_execz .LBB0_58
	v_lshlrev_b32_e32 v9, 8, v9
	v_and_b32_e32 v8, 0xf0, v8
	v_add3_u32 v8, s84, v9, v8
	ds_read_b128 v[8:11], v8
	v_add_lshl_u32 v2, v2, s76, 10
	v_lshl_add_u64 v[12:13], v[2:3], 2, v[4:5]
	s_waitcnt lgkmcnt(0)
	global_store_dwordx4 v[12:13], v[8:11], off sc0 sc1
.LBB0_58:
	s_or_b64 exec, exec, s[4:5]
	s_nop 0
	v_add_u32_e32 v8, 20, v7
	v_add_u32_e32 v2, s88, v8
	v_cmp_gt_i32_e32 vcc, s3, v2
	s_and_saveexec_b64 s[4:5], vcc
	s_cbranch_execz .LBB0_60
	v_lshlrev_b32_e32 v9, 8, v8
	v_xor_b32_e32 v8, v8, v6
	v_lshlrev_b32_e32 v8, 4, v8
	v_and_b32_e32 v8, 0xf0, v8
	v_add3_u32 v8, s84, v9, v8
	ds_read_b128 v[8:11], v8
	v_add_lshl_u32 v2, v2, s76, 10
	v_lshl_add_u64 v[12:13], v[2:3], 2, v[4:5]
	s_waitcnt lgkmcnt(0)
	global_store_dwordx4 v[12:13], v[8:11], off sc0 sc1
.LBB0_60:
	s_or_b64 exec, exec, s[4:5]
	s_nop 0
	v_add_u32_e32 v8, 24, v7
	v_add_u32_e32 v2, s88, v8
	v_cmp_gt_i32_e32 vcc, s3, v2
	s_and_saveexec_b64 s[4:5], vcc
	s_cbranch_execz .LBB0_62
	v_lshlrev_b32_e32 v9, 8, v8
	v_xor_b32_e32 v8, v8, v6
	v_lshlrev_b32_e32 v8, 4, v8
	v_and_b32_e32 v8, 0xf0, v8
	v_add3_u32 v8, s84, v9, v8
	ds_read_b128 v[8:11], v8
	v_add_lshl_u32 v2, v2, s76, 10
	v_lshl_add_u64 v[12:13], v[2:3], 2, v[4:5]
	s_waitcnt lgkmcnt(0)
	global_store_dwordx4 v[12:13], v[8:11], off sc0 sc1
.LBB0_62:
	s_or_b64 exec, exec, s[4:5]
	v_add_u32_e32 v7, 28, v7
	v_add_u32_e32 v2, s88, v7
	v_cmp_gt_i32_e32 vcc, s3, v2
	s_and_saveexec_b64 s[4:5], vcc
	s_cbranch_execz .LBB0_4
	v_xor_b32_e32 v6, v7, v6
	v_lshlrev_b32_e32 v6, 4, v6
	v_lshlrev_b32_e32 v8, 8, v7
	v_and_b32_e32 v6, 0xf0, v6
	v_add3_u32 v6, s84, v8, v6
	ds_read_b128 v[6:9], v6
	v_add_lshl_u32 v2, v2, s76, 10
	v_lshl_add_u64 v[4:5], v[2:3], 2, v[4:5]
	s_waitcnt lgkmcnt(0)
	global_store_dwordx4 v[4:5], v[6:9], off sc0 sc1
	s_branch .LBB0_4
